# sel block head: the tile's first six K ds_reads are issued before the next-triple DMA stub, so the stub's scalar work and DMA issue hide the LDS latency
# speedup vs baseline: 1.0083x; 1.0083x over previous
; #define RING_BARRIER() do { asm volatile("s_waitcnt lgkmcnt(0)" ::: "memory"); __builtin_amdgcn_s_barrier(); asm volatile("" ::: "memory"); } while (0)
; #define RD16(dst, base, off) asm volatile("ds_read_b128 %0, %1 offset:%2" : "=&v"(dst) : "v"(base), "i"(off) : "memory")
; __device__ __forceinline__ void qk8_tile_c(f32x4 (&s)[4], const GS8& g, const unsigned kb  , const float c0  ) {
;     i32x4a lo[4], hi[4];
;     RD16(lo[0], kb, 0); RD16(hi[0], kb, 16); RD16(lo[1], kb, 16 * K8ST); RD16(hi[1], kb, 16 * K8ST + 16);
;     RD16(lo[2], kb, 32 * K8ST); RD16(hi[2], kb, 32 * K8ST + 16); RD16(lo[3], kb, 48 * K8ST); RD16(hi[3], kb, 48 * K8ST + 16);
; template <bool DUMMY> __device__ __forceinline__ void sel_phase(Frame& F) {
;     ...
;         SEL_DMA3(cj, F.lds);
;         for (int p = 0; p < npair; ++p) {
;             u32x2 dnx = {0xffffffffu, 0u}; if (p + 1 < npair) dnx = PD[(p + 1) * 8 + F.wave];
;             asm volatile("s_waitcnt vmcnt(0)" ::: "memory"); RING_BARRIER();
;             const unsigned nj = (unsigned)__builtin_amdgcn_readfirstlane((int)dnx.x), nb = (unsigned)__builtin_amdgcn_readfirstlane((int)dnx.y);
;             if (p + 1 < npair && !(DUMMY && MK_EXP == 2)) { SEL_DMA3(nj, F.lds + ((p + 1) & 1) * 3 * SLOTS); }
.Lsel_tile:
	ds_read_b128 v[84:87], v208 offset:0
	ds_read_b128 v[88:91], v208 offset:16
	ds_read_b128 v[92:95], v208 offset:0x900
	ds_read_b128 v[96:99], v208 offset:0x910
	ds_read_b128 v[118:121], v208 offset:0x1200
	ds_read_b128 v[122:125], v208 offset:0x1210
	s_bitcmp1_b32 s99, s37
	s_cbranch_scc0 .Lsel_tile2
	s_lshr_b32 vcc_lo, s60, s36
	s_and_b32 vcc_lo, vcc_lo, 0xff
	s_lshl_b32 vcc_lo, vcc_lo, 13
	s_add_u32 s12, s62, vcc_lo
	s_addc_u32 s13, s63, 0
	s_add_u32 s100, s64, vcc_lo
	s_addc_u32 s101, s65, 0
	s_mul_i32 vcc_hi, s37, 0x4c00
	s_add_i32 vcc_hi, s98, vcc_hi
	s_mov_b32 m0, vcc_hi
	s_cmp_lg_u64 s[16:17], 0
	global_load_lds_dwordx4 v102, s[12:13]
	s_cselect_b32 s13, s13, s101
	s_cselect_b32 s12, s12, s100
	s_add_i32 m0, vcc_hi, 0x2000
	s_cmp_lg_u64 s[10:11], 0
	global_load_lds_dwordx4 v106, s[12:13]
	s_cbranch_scc1 .Lsel_tile2
	s_add_i32 m0, vcc_hi, 0x4000
	s_nop 0
	global_load_lds_dwordx4 v108, s[100:101]
.Lsel_tile2:
	s_and_b32 vcc_lo, s45, 15
	s_cbranch_scc0 .Lsel_g1_pre
	v_and_b32_e32 v18, s45, v154
	v_cmp_eq_u32_e32 vcc, 0, v18
	s_lshr_b32 s44, s66, s36
	s_and_b32 s44, s44, 0xff
	v_cndmask_b32_e32 v210, v216, v181, vcc
	v_mov_b32_e32 v211, v210
	v_mov_b32_e32 v212, v210
	v_mov_b32_e32 v213, v210
	ds_read_b128 v[126:129], v208 offset:0x1b00
	ds_read_b128 v[130:133], v208 offset:0x1b10
	s_waitcnt lgkmcnt(6)
	v_mfma_scale_f32_16x16x128_f8f6f4 v[84:87], v[84:91], v[0:7], v[210:213], v178, v177 op_sel_hi:[0,0,0]
	ds_read_b128 v[134:137], v207 offset:0
	ds_read_b128 v[138:141], v207 offset:0x500
	ds_read_b128 v[142:145], v207 offset:0xa00
	ds_read_b128 v[146:149], v207 offset:0xf00
	s_waitcnt lgkmcnt(8)
	v_mfma_scale_f32_16x16x128_f8f6f4 v[88:91], v[92:99], v[0:7], v[210:213], v178, v177 op_sel_hi:[0,0,0]
	s_waitcnt lgkmcnt(6)
	v_mfma_scale_f32_16x16x128_f8f6f4 v[92:95], v[118:125], v[0:7], v[210:213], v178, v177 op_sel_hi:[0,0,0]
	s_waitcnt lgkmcnt(4)
	v_mfma_scale_f32_16x16x128_f8f6f4 v[96:99], v[126:133], v[0:7], v[210:213], v178, v177 op_sel_hi:[0,0,0]
	ds_read_b128 v[118:121], v207 offset:0x1400
	ds_read_b128 v[122:125], v207 offset:0x1900
	ds_read_b128 v[126:129], v207 offset:0x1e00
	ds_read_b128 v[130:133], v207 offset:0x2300
	s_cmp_eq_u32 s44, s58
	s_cbranch_scc1 .Lsel_diag_g0
